# speedup vs baseline: 1.0253x; 1.0036x over previous
_Z5k_csrPKiS0_PiS1_PKfS3_S3_S3_PDF16_P15HIP_vector_typeIfLj4EES7_:
	s_cmpk_lt_u32 s2, 0x187
	s_mov_b64 s[4:5], -1
	s_cbranch_scc0 .LBB2_75
	s_mov_b32 s27, s2
	s_load_dwordx8 s[28:35], s[0:1], 0x20
	s_load_dwordx2 s[36:37], s[0:1], 0x40
	v_lshrrev_b32_e32 v56, 6, v0
	v_and_b32_e32 v57, 63, v0
	s_nop 0
	v_readfirstlane_b32 s62, v56
	s_and_b32 s63, s62, 3
	s_lshr_b32 s62, s62, 2
	s_lshl_b32 s62, s62, 6
	v_add_u32_e32 v58, s62, v57
	s_lshl_b32 s62, s2, 8
	v_add_u32_e32 v59, s62, v58
	s_mov_b32 s62, 0x186a0
	v_cmp_gt_i32_e64 s[40:41], s62, v59
	s_and_saveexec_b64 s[38:39], s[40:41]
	s_cbranch_execz .Lc7_nox
	v_mul_u32_u24_e32 v60, 40, v59
	s_waitcnt lgkmcnt(0)
	global_load_dwordx4 v[32:35], v60, s[28:29]
	global_load_dwordx4 v[36:39], v60, s[28:29] offset:16
	global_load_dwordx2 v[40:41], v60, s[28:29] offset:32
.Lc7_nox:
	s_or_b64 exec, exec, s[38:39]
	s_waitcnt lgkmcnt(0)
	s_load_dwordx4 s[12:15], s[0:1], 0x0
	s_mov_b32 s3, 0
	s_lshl_b64 s[4:5], s[2:3], 2
	s_movk_i32 s3, 0x100
	v_cmp_gt_u32_e32 vcc, s3, v0
	s_waitcnt lgkmcnt(0)
	s_add_u32 s4, s12, s4
	s_addc_u32 s5, s13, s5
	s_load_dwordx2 s[16:17], s[4:5], 0x0
	s_and_saveexec_b64 s[4:5], vcc
	v_lshlrev_b32_e32 v1, 2, v0
	v_mov_b32_e32 v2, 0
	ds_write_b32 v1, v2 offset:4864
	s_or_b64 exec, exec, s[4:5]
	s_waitcnt lgkmcnt(0)
	v_add_u32_e32 v2, s16, v0
	v_cmp_gt_i32_e64 s[4:5], s17, v2
	v_mov_b32_e32 v8, -1
	v_mov_b32_e32 v9, -1
	s_barrier
	s_waitcnt vmcnt(0)
	s_and_saveexec_b64 s[6:7], s[4:5]
	s_cbranch_execz .LBB2_5
	v_ashrrev_i32_e32 v3, 31, v2
	v_lshl_add_u64 v[4:5], v[2:3], 2, s[14:15]
	global_load_dword v9, v[4:5], off

.Lc5_ld:
	s_or_b64 exec, exec, s[6:7]
	v_add_u32_e32 v4, 0xc00, v2
	v_cmp_gt_i32_e64 s[4:5], s17, v4
	s_and_saveexec_b64 s[6:7], s[4:5]
	s_cbranch_execz .Lc7_l4
	v_ashrrev_i32_e32 v5, 31, v4
	v_lshl_add_u64 v[4:5], v[4:5], 2, s[14:15]
	global_load_dword v1, v[4:5], off
.Lc7_l4:
	s_or_b64 exec, exec, s[6:7]
	s_and_saveexec_b64 s[38:39], s[40:41]
	s_cbranch_execz .Ln0b_skip
	s_lshl_b32 s62, s63, 6
	s_add_u32 s30, s30, s62
	s_addc_u32 s31, s31, 0
	s_add_u32 s32, s32, s62
	s_addc_u32 s33, s33, 0
	s_lshl_b32 s62, s63, 9
	s_add_u32 s34, s34, s62
	s_addc_u32 s35, s35, 0
	s_lshl_b32 s62, s63, 5
	v_lshlrev_b32_e32 v60, 7, v59
	v_add_u32_e32 v60, s62, v60
	v_lshlrev_b32_e32 v61, 7, v58
	v_add_u32_e32 v61, s62, v61
	v_add_u32_e32 v61, 0x1740, v61
	v_mov_b32_e32 v44, 0
	v_mov_b32_e32 v45, 0
	v_mov_b32_e32 v46, 0
	v_mov_b32_e32 v47, 0
	v_mov_b32_e32 v48, 0
	v_mov_b32_e32 v49, 0
	v_mov_b32_e32 v50, 0
	v_mov_b32_e32 v51, 0
	s_load_dwordx2 s[40:41], s[30:31], 0x0
	s_load_dwordx2 s[42:43], s[30:31], 0x100
	s_load_dwordx2 s[44:45], s[30:31], 0x200
	s_load_dwordx2 s[46:47], s[30:31], 0x300
	s_load_dwordx2 s[48:49], s[30:31], 0x400
	s_load_dwordx2 s[50:51], s[30:31], 0x500
	s_load_dwordx2 s[52:53], s[30:31], 0x600
	s_load_dwordx2 s[54:55], s[30:31], 0x700
	s_load_dwordx2 s[56:57], s[30:31], 0x800
	s_load_dwordx2 s[58:59], s[30:31], 0x900
	s_load_dwordx2 s[60:61], s[32:33], 0x0
	s_load_dwordx16 s[64:79], s[34:35], 0x0
	s_waitcnt lgkmcnt(0)
	v_mov_b32_e32 v42, s60
	v_mov_b32_e32 v43, s61
	v_pk_fma_f32 v[42:43], v[32:33], s[40:41], v[42:43] op_sel_hi:[0,1,1]
	v_pk_fma_f32 v[42:43], v[32:33], s[42:43], v[42:43] op_sel:[1,0,0]
	v_pk_fma_f32 v[42:43], v[34:35], s[44:45], v[42:43] op_sel_hi:[0,1,1]
	v_pk_fma_f32 v[42:43], v[34:35], s[46:47], v[42:43] op_sel:[1,0,0]
	v_pk_fma_f32 v[42:43], v[36:37], s[48:49], v[42:43] op_sel_hi:[0,1,1]
	v_pk_fma_f32 v[42:43], v[36:37], s[50:51], v[42:43] op_sel:[1,0,0]
	v_pk_fma_f32 v[42:43], v[38:39], s[52:53], v[42:43] op_sel_hi:[0,1,1]
	v_pk_fma_f32 v[42:43], v[38:39], s[54:55], v[42:43] op_sel:[1,0,0]
	v_pk_fma_f32 v[42:43], v[40:41], s[56:57], v[42:43] op_sel_hi:[0,1,1]
	v_pk_fma_f32 v[42:43], v[40:41], s[58:59], v[42:43] op_sel:[1,0,0]
	v_max_f32_e32 v42, 0, v42
	v_max_f32_e32 v43, 0, v43
	v_cvt_pk_f16_f32 v52, v42, v43
	v_pk_fma_f32 v[44:45], v[42:43], s[64:65], v[44:45] op_sel_hi:[0,1,1]
	v_pk_fma_f32 v[46:47], v[42:43], s[66:67], v[46:47] op_sel_hi:[0,1,1]
	v_pk_fma_f32 v[48:49], v[42:43], s[68:69], v[48:49] op_sel_hi:[0,1,1]
	v_pk_fma_f32 v[50:51], v[42:43], s[70:71], v[50:51] op_sel_hi:[0,1,1]
	v_pk_fma_f32 v[44:45], v[42:43], s[72:73], v[44:45] op_sel:[1,0,0]
	v_pk_fma_f32 v[46:47], v[42:43], s[74:75], v[46:47] op_sel:[1,0,0]
	v_pk_fma_f32 v[48:49], v[42:43], s[76:77], v[48:49] op_sel:[1,0,0]
	v_pk_fma_f32 v[50:51], v[42:43], s[78:79], v[50:51] op_sel:[1,0,0]
	s_load_dwordx2 s[40:41], s[30:31], 0x8
	s_load_dwordx2 s[42:43], s[30:31], 0x108
	s_load_dwordx2 s[44:45], s[30:31], 0x208
	s_load_dwordx2 s[46:47], s[30:31], 0x308
	s_load_dwordx2 s[48:49], s[30:31], 0x408
	s_load_dwordx2 s[50:51], s[30:31], 0x508
	s_load_dwordx2 s[52:53], s[30:31], 0x608
	s_load_dwordx2 s[54:55], s[30:31], 0x708
	s_load_dwordx2 s[56:57], s[30:31], 0x808
	s_load_dwordx2 s[58:59], s[30:31], 0x908
	s_load_dwordx2 s[60:61], s[32:33], 0x8
	s_load_dwordx16 s[64:79], s[34:35], 0x40
	s_waitcnt lgkmcnt(0)
	v_mov_b32_e32 v42, s60
	v_mov_b32_e32 v43, s61
	v_pk_fma_f32 v[42:43], v[32:33], s[40:41], v[42:43] op_sel_hi:[0,1,1]
	v_pk_fma_f32 v[42:43], v[32:33], s[42:43], v[42:43] op_sel:[1,0,0]
	v_pk_fma_f32 v[42:43], v[34:35], s[44:45], v[42:43] op_sel_hi:[0,1,1]
	v_pk_fma_f32 v[42:43], v[34:35], s[46:47], v[42:43] op_sel:[1,0,0]
	v_pk_fma_f32 v[42:43], v[36:37], s[48:49], v[42:43] op_sel_hi:[0,1,1]
	v_pk_fma_f32 v[42:43], v[36:37], s[50:51], v[42:43] op_sel:[1,0,0]
	v_pk_fma_f32 v[42:43], v[38:39], s[52:53], v[42:43] op_sel_hi:[0,1,1]
	v_pk_fma_f32 v[42:43], v[38:39], s[54:55], v[42:43] op_sel:[1,0,0]
	v_pk_fma_f32 v[42:43], v[40:41], s[56:57], v[42:43] op_sel_hi:[0,1,1]
	v_pk_fma_f32 v[42:43], v[40:41], s[58:59], v[42:43] op_sel:[1,0,0]
	v_max_f32_e32 v42, 0, v42
	v_max_f32_e32 v43, 0, v43
	v_cvt_pk_f16_f32 v53, v42, v43
	v_pk_fma_f32 v[44:45], v[42:43], s[64:65], v[44:45] op_sel_hi:[0,1,1]
	v_pk_fma_f32 v[46:47], v[42:43], s[66:67], v[46:47] op_sel_hi:[0,1,1]
	v_pk_fma_f32 v[48:49], v[42:43], s[68:69], v[48:49] op_sel_hi:[0,1,1]
	v_pk_fma_f32 v[50:51], v[42:43], s[70:71], v[50:51] op_sel_hi:[0,1,1]
	v_pk_fma_f32 v[44:45], v[42:43], s[72:73], v[44:45] op_sel:[1,0,0]
	v_pk_fma_f32 v[46:47], v[42:43], s[74:75], v[46:47] op_sel:[1,0,0]
	v_pk_fma_f32 v[48:49], v[42:43], s[76:77], v[48:49] op_sel:[1,0,0]
	v_pk_fma_f32 v[50:51], v[42:43], s[78:79], v[50:51] op_sel:[1,0,0]
	s_load_dwordx2 s[40:41], s[30:31], 0x10
	s_load_dwordx2 s[42:43], s[30:31], 0x110
	s_load_dwordx2 s[44:45], s[30:31], 0x210
	s_load_dwordx2 s[46:47], s[30:31], 0x310
	s_load_dwordx2 s[48:49], s[30:31], 0x410
	s_load_dwordx2 s[50:51], s[30:31], 0x510
	s_load_dwordx2 s[52:53], s[30:31], 0x610
	s_load_dwordx2 s[54:55], s[30:31], 0x710
	s_load_dwordx2 s[56:57], s[30:31], 0x810
	s_load_dwordx2 s[58:59], s[30:31], 0x910
	s_load_dwordx2 s[60:61], s[32:33], 0x10
	s_load_dwordx16 s[64:79], s[34:35], 0x80
	s_waitcnt lgkmcnt(0)
	v_mov_b32_e32 v42, s60
	v_mov_b32_e32 v43, s61
	v_pk_fma_f32 v[42:43], v[32:33], s[40:41], v[42:43] op_sel_hi:[0,1,1]
	v_pk_fma_f32 v[42:43], v[32:33], s[42:43], v[42:43] op_sel:[1,0,0]
	v_pk_fma_f32 v[42:43], v[34:35], s[44:45], v[42:43] op_sel_hi:[0,1,1]
	v_pk_fma_f32 v[42:43], v[34:35], s[46:47], v[42:43] op_sel:[1,0,0]
	v_pk_fma_f32 v[42:43], v[36:37], s[48:49], v[42:43] op_sel_hi:[0,1,1]
	v_pk_fma_f32 v[42:43], v[36:37], s[50:51], v[42:43] op_sel:[1,0,0]
	v_pk_fma_f32 v[42:43], v[38:39], s[52:53], v[42:43] op_sel_hi:[0,1,1]
	v_pk_fma_f32 v[42:43], v[38:39], s[54:55], v[42:43] op_sel:[1,0,0]
	v_pk_fma_f32 v[42:43], v[40:41], s[56:57], v[42:43] op_sel_hi:[0,1,1]
	v_pk_fma_f32 v[42:43], v[40:41], s[58:59], v[42:43] op_sel:[1,0,0]
	v_max_f32_e32 v42, 0, v42
	v_max_f32_e32 v43, 0, v43
	v_cvt_pk_f16_f32 v54, v42, v43
	v_pk_fma_f32 v[44:45], v[42:43], s[64:65], v[44:45] op_sel_hi:[0,1,1]
	v_pk_fma_f32 v[46:47], v[42:43], s[66:67], v[46:47] op_sel_hi:[0,1,1]
	v_pk_fma_f32 v[48:49], v[42:43], s[68:69], v[48:49] op_sel_hi:[0,1,1]
	v_pk_fma_f32 v[50:51], v[42:43], s[70:71], v[50:51] op_sel_hi:[0,1,1]
	v_pk_fma_f32 v[44:45], v[42:43], s[72:73], v[44:45] op_sel:[1,0,0]
	v_pk_fma_f32 v[46:47], v[42:43], s[74:75], v[46:47] op_sel:[1,0,0]
	v_pk_fma_f32 v[48:49], v[42:43], s[76:77], v[48:49] op_sel:[1,0,0]
	v_pk_fma_f32 v[50:51], v[42:43], s[78:79], v[50:51] op_sel:[1,0,0]
	s_load_dwordx2 s[40:41], s[30:31], 0x18
	s_load_dwordx2 s[42:43], s[30:31], 0x118
	s_load_dwordx2 s[44:45], s[30:31], 0x218
	s_load_dwordx2 s[46:47], s[30:31], 0x318
	s_load_dwordx2 s[48:49], s[30:31], 0x418
	s_load_dwordx2 s[50:51], s[30:31], 0x518
	s_load_dwordx2 s[52:53], s[30:31], 0x618
	s_load_dwordx2 s[54:55], s[30:31], 0x718
	s_load_dwordx2 s[56:57], s[30:31], 0x818
	s_load_dwordx2 s[58:59], s[30:31], 0x918
	s_load_dwordx2 s[60:61], s[32:33], 0x18
	s_load_dwordx16 s[64:79], s[34:35], 0xc0
	s_waitcnt lgkmcnt(0)
	v_mov_b32_e32 v42, s60
	v_mov_b32_e32 v43, s61
	v_pk_fma_f32 v[42:43], v[32:33], s[40:41], v[42:43] op_sel_hi:[0,1,1]
	v_pk_fma_f32 v[42:43], v[32:33], s[42:43], v[42:43] op_sel:[1,0,0]
	v_pk_fma_f32 v[42:43], v[34:35], s[44:45], v[42:43] op_sel_hi:[0,1,1]
	v_pk_fma_f32 v[42:43], v[34:35], s[46:47], v[42:43] op_sel:[1,0,0]
	v_pk_fma_f32 v[42:43], v[36:37], s[48:49], v[42:43] op_sel_hi:[0,1,1]
	v_pk_fma_f32 v[42:43], v[36:37], s[50:51], v[42:43] op_sel:[1,0,0]
	v_pk_fma_f32 v[42:43], v[38:39], s[52:53], v[42:43] op_sel_hi:[0,1,1]
	v_pk_fma_f32 v[42:43], v[38:39], s[54:55], v[42:43] op_sel:[1,0,0]
	v_pk_fma_f32 v[42:43], v[40:41], s[56:57], v[42:43] op_sel_hi:[0,1,1]
	v_pk_fma_f32 v[42:43], v[40:41], s[58:59], v[42:43] op_sel:[1,0,0]
	v_max_f32_e32 v42, 0, v42
	v_max_f32_e32 v43, 0, v43
	v_cvt_pk_f16_f32 v55, v42, v43
	v_pk_fma_f32 v[44:45], v[42:43], s[64:65], v[44:45] op_sel_hi:[0,1,1]
	v_pk_fma_f32 v[46:47], v[42:43], s[66:67], v[46:47] op_sel_hi:[0,1,1]
	v_pk_fma_f32 v[48:49], v[42:43], s[68:69], v[48:49] op_sel_hi:[0,1,1]
	v_pk_fma_f32 v[50:51], v[42:43], s[70:71], v[50:51] op_sel_hi:[0,1,1]
	v_pk_fma_f32 v[44:45], v[42:43], s[72:73], v[44:45] op_sel:[1,0,0]
	v_pk_fma_f32 v[46:47], v[42:43], s[74:75], v[46:47] op_sel:[1,0,0]
	v_pk_fma_f32 v[48:49], v[42:43], s[76:77], v[48:49] op_sel:[1,0,0]
	v_pk_fma_f32 v[50:51], v[42:43], s[78:79], v[50:51] op_sel:[1,0,0]
	global_store_dwordx4 v60, v[52:55], s[36:37] offset:0
	s_load_dwordx2 s[40:41], s[30:31], 0x20
	s_load_dwordx2 s[42:43], s[30:31], 0x120
	s_load_dwordx2 s[44:45], s[30:31], 0x220
	s_load_dwordx2 s[46:47], s[30:31], 0x320
	s_load_dwordx2 s[48:49], s[30:31], 0x420
	s_load_dwordx2 s[50:51], s[30:31], 0x520
	s_load_dwordx2 s[52:53], s[30:31], 0x620
	s_load_dwordx2 s[54:55], s[30:31], 0x720
	s_load_dwordx2 s[56:57], s[30:31], 0x820
	s_load_dwordx2 s[58:59], s[30:31], 0x920
	s_load_dwordx2 s[60:61], s[32:33], 0x20
	s_load_dwordx16 s[64:79], s[34:35], 0x100
	s_waitcnt lgkmcnt(0)
	v_mov_b32_e32 v42, s60
	v_mov_b32_e32 v43, s61
	v_pk_fma_f32 v[42:43], v[32:33], s[40:41], v[42:43] op_sel_hi:[0,1,1]
	v_pk_fma_f32 v[42:43], v[32:33], s[42:43], v[42:43] op_sel:[1,0,0]
	v_pk_fma_f32 v[42:43], v[34:35], s[44:45], v[42:43] op_sel_hi:[0,1,1]
	v_pk_fma_f32 v[42:43], v[34:35], s[46:47], v[42:43] op_sel:[1,0,0]
	v_pk_fma_f32 v[42:43], v[36:37], s[48:49], v[42:43] op_sel_hi:[0,1,1]
	v_pk_fma_f32 v[42:43], v[36:37], s[50:51], v[42:43] op_sel:[1,0,0]
	v_pk_fma_f32 v[42:43], v[38:39], s[52:53], v[42:43] op_sel_hi:[0,1,1]
	v_pk_fma_f32 v[42:43], v[38:39], s[54:55], v[42:43] op_sel:[1,0,0]
	v_pk_fma_f32 v[42:43], v[40:41], s[56:57], v[42:43] op_sel_hi:[0,1,1]
	v_pk_fma_f32 v[42:43], v[40:41], s[58:59], v[42:43] op_sel:[1,0,0]
	v_max_f32_e32 v42, 0, v42
	v_max_f32_e32 v43, 0, v43
	v_cvt_pk_f16_f32 v52, v42, v43
	v_pk_fma_f32 v[44:45], v[42:43], s[64:65], v[44:45] op_sel_hi:[0,1,1]
	v_pk_fma_f32 v[46:47], v[42:43], s[66:67], v[46:47] op_sel_hi:[0,1,1]
	v_pk_fma_f32 v[48:49], v[42:43], s[68:69], v[48:49] op_sel_hi:[0,1,1]
	v_pk_fma_f32 v[50:51], v[42:43], s[70:71], v[50:51] op_sel_hi:[0,1,1]
	v_pk_fma_f32 v[44:45], v[42:43], s[72:73], v[44:45] op_sel:[1,0,0]
	v_pk_fma_f32 v[46:47], v[42:43], s[74:75], v[46:47] op_sel:[1,0,0]
	v_pk_fma_f32 v[48:49], v[42:43], s[76:77], v[48:49] op_sel:[1,0,0]
	v_pk_fma_f32 v[50:51], v[42:43], s[78:79], v[50:51] op_sel:[1,0,0]
	s_load_dwordx2 s[40:41], s[30:31], 0x28
	s_load_dwordx2 s[42:43], s[30:31], 0x128
	s_load_dwordx2 s[44:45], s[30:31], 0x228
	s_load_dwordx2 s[46:47], s[30:31], 0x328
	s_load_dwordx2 s[48:49], s[30:31], 0x428
	s_load_dwordx2 s[50:51], s[30:31], 0x528
	s_load_dwordx2 s[52:53], s[30:31], 0x628
	s_load_dwordx2 s[54:55], s[30:31], 0x728
	s_load_dwordx2 s[56:57], s[30:31], 0x828
	s_load_dwordx2 s[58:59], s[30:31], 0x928
	s_load_dwordx2 s[60:61], s[32:33], 0x28
	s_load_dwordx16 s[64:79], s[34:35], 0x140
	s_waitcnt lgkmcnt(0)
	v_mov_b32_e32 v42, s60
	v_mov_b32_e32 v43, s61
	v_pk_fma_f32 v[42:43], v[32:33], s[40:41], v[42:43] op_sel_hi:[0,1,1]
	v_pk_fma_f32 v[42:43], v[32:33], s[42:43], v[42:43] op_sel:[1,0,0]
	v_pk_fma_f32 v[42:43], v[34:35], s[44:45], v[42:43] op_sel_hi:[0,1,1]
	v_pk_fma_f32 v[42:43], v[34:35], s[46:47], v[42:43] op_sel:[1,0,0]
	v_pk_fma_f32 v[42:43], v[36:37], s[48:49], v[42:43] op_sel_hi:[0,1,1]
	v_pk_fma_f32 v[42:43], v[36:37], s[50:51], v[42:43] op_sel:[1,0,0]
	v_pk_fma_f32 v[42:43], v[38:39], s[52:53], v[42:43] op_sel_hi:[0,1,1]
	v_pk_fma_f32 v[42:43], v[38:39], s[54:55], v[42:43] op_sel:[1,0,0]
	v_pk_fma_f32 v[42:43], v[40:41], s[56:57], v[42:43] op_sel_hi:[0,1,1]
	v_pk_fma_f32 v[42:43], v[40:41], s[58:59], v[42:43] op_sel:[1,0,0]
	v_max_f32_e32 v42, 0, v42
	v_max_f32_e32 v43, 0, v43
	v_cvt_pk_f16_f32 v53, v42, v43
	v_pk_fma_f32 v[44:45], v[42:43], s[64:65], v[44:45] op_sel_hi:[0,1,1]
	v_pk_fma_f32 v[46:47], v[42:43], s[66:67], v[46:47] op_sel_hi:[0,1,1]
	v_pk_fma_f32 v[48:49], v[42:43], s[68:69], v[48:49] op_sel_hi:[0,1,1]
	v_pk_fma_f32 v[50:51], v[42:43], s[70:71], v[50:51] op_sel_hi:[0,1,1]
	v_pk_fma_f32 v[44:45], v[42:43], s[72:73], v[44:45] op_sel:[1,0,0]
	v_pk_fma_f32 v[46:47], v[42:43], s[74:75], v[46:47] op_sel:[1,0,0]
	v_pk_fma_f32 v[48:49], v[42:43], s[76:77], v[48:49] op_sel:[1,0,0]
	v_pk_fma_f32 v[50:51], v[42:43], s[78:79], v[50:51] op_sel:[1,0,0]
	s_load_dwordx2 s[40:41], s[30:31], 0x30
	s_load_dwordx2 s[42:43], s[30:31], 0x130
	s_load_dwordx2 s[44:45], s[30:31], 0x230
	s_load_dwordx2 s[46:47], s[30:31], 0x330
	s_load_dwordx2 s[48:49], s[30:31], 0x430
	s_load_dwordx2 s[50:51], s[30:31], 0x530
	s_load_dwordx2 s[52:53], s[30:31], 0x630
	s_load_dwordx2 s[54:55], s[30:31], 0x730
	s_load_dwordx2 s[56:57], s[30:31], 0x830
	s_load_dwordx2 s[58:59], s[30:31], 0x930
	s_load_dwordx2 s[60:61], s[32:33], 0x30
	s_load_dwordx16 s[64:79], s[34:35], 0x180
	s_waitcnt lgkmcnt(0)
	v_mov_b32_e32 v42, s60
	v_mov_b32_e32 v43, s61
	v_pk_fma_f32 v[42:43], v[32:33], s[40:41], v[42:43] op_sel_hi:[0,1,1]
	v_pk_fma_f32 v[42:43], v[32:33], s[42:43], v[42:43] op_sel:[1,0,0]
	v_pk_fma_f32 v[42:43], v[34:35], s[44:45], v[42:43] op_sel_hi:[0,1,1]
	v_pk_fma_f32 v[42:43], v[34:35], s[46:47], v[42:43] op_sel:[1,0,0]
	v_pk_fma_f32 v[42:43], v[36:37], s[48:49], v[42:43] op_sel_hi:[0,1,1]
	v_pk_fma_f32 v[42:43], v[36:37], s[50:51], v[42:43] op_sel:[1,0,0]
	v_pk_fma_f32 v[42:43], v[38:39], s[52:53], v[42:43] op_sel_hi:[0,1,1]
	v_pk_fma_f32 v[42:43], v[38:39], s[54:55], v[42:43] op_sel:[1,0,0]
	v_pk_fma_f32 v[42:43], v[40:41], s[56:57], v[42:43] op_sel_hi:[0,1,1]
	v_pk_fma_f32 v[42:43], v[40:41], s[58:59], v[42:43] op_sel:[1,0,0]
	v_max_f32_e32 v42, 0, v42
	v_max_f32_e32 v43, 0, v43
	v_cvt_pk_f16_f32 v54, v42, v43
	v_pk_fma_f32 v[44:45], v[42:43], s[64:65], v[44:45] op_sel_hi:[0,1,1]
	v_pk_fma_f32 v[46:47], v[42:43], s[66:67], v[46:47] op_sel_hi:[0,1,1]
	v_pk_fma_f32 v[48:49], v[42:43], s[68:69], v[48:49] op_sel_hi:[0,1,1]
	v_pk_fma_f32 v[50:51], v[42:43], s[70:71], v[50:51] op_sel_hi:[0,1,1]
	v_pk_fma_f32 v[44:45], v[42:43], s[72:73], v[44:45] op_sel:[1,0,0]
	v_pk_fma_f32 v[46:47], v[42:43], s[74:75], v[46:47] op_sel:[1,0,0]
	v_pk_fma_f32 v[48:49], v[42:43], s[76:77], v[48:49] op_sel:[1,0,0]
	v_pk_fma_f32 v[50:51], v[42:43], s[78:79], v[50:51] op_sel:[1,0,0]
	s_load_dwordx2 s[40:41], s[30:31], 0x38
	s_load_dwordx2 s[42:43], s[30:31], 0x138
	s_load_dwordx2 s[44:45], s[30:31], 0x238
	s_load_dwordx2 s[46:47], s[30:31], 0x338
	s_load_dwordx2 s[48:49], s[30:31], 0x438
	s_load_dwordx2 s[50:51], s[30:31], 0x538
	s_load_dwordx2 s[52:53], s[30:31], 0x638
	s_load_dwordx2 s[54:55], s[30:31], 0x738
	s_load_dwordx2 s[56:57], s[30:31], 0x838
	s_load_dwordx2 s[58:59], s[30:31], 0x938
	s_load_dwordx2 s[60:61], s[32:33], 0x38
	s_load_dwordx16 s[64:79], s[34:35], 0x1c0
	s_waitcnt lgkmcnt(0)
	v_mov_b32_e32 v42, s60
	v_mov_b32_e32 v43, s61
	v_pk_fma_f32 v[42:43], v[32:33], s[40:41], v[42:43] op_sel_hi:[0,1,1]
	v_pk_fma_f32 v[42:43], v[32:33], s[42:43], v[42:43] op_sel:[1,0,0]
	v_pk_fma_f32 v[42:43], v[34:35], s[44:45], v[42:43] op_sel_hi:[0,1,1]
	v_pk_fma_f32 v[42:43], v[34:35], s[46:47], v[42:43] op_sel:[1,0,0]
	v_pk_fma_f32 v[42:43], v[36:37], s[48:49], v[42:43] op_sel_hi:[0,1,1]
	v_pk_fma_f32 v[42:43], v[36:37], s[50:51], v[42:43] op_sel:[1,0,0]
	v_pk_fma_f32 v[42:43], v[38:39], s[52:53], v[42:43] op_sel_hi:[0,1,1]
	v_pk_fma_f32 v[42:43], v[38:39], s[54:55], v[42:43] op_sel:[1,0,0]
	v_pk_fma_f32 v[42:43], v[40:41], s[56:57], v[42:43] op_sel_hi:[0,1,1]
	v_pk_fma_f32 v[42:43], v[40:41], s[58:59], v[42:43] op_sel:[1,0,0]
	v_max_f32_e32 v42, 0, v42
	v_max_f32_e32 v43, 0, v43
	v_cvt_pk_f16_f32 v55, v42, v43
	v_pk_fma_f32 v[44:45], v[42:43], s[64:65], v[44:45] op_sel_hi:[0,1,1]
	v_pk_fma_f32 v[46:47], v[42:43], s[66:67], v[46:47] op_sel_hi:[0,1,1]
	v_pk_fma_f32 v[48:49], v[42:43], s[68:69], v[48:49] op_sel_hi:[0,1,1]
	v_pk_fma_f32 v[50:51], v[42:43], s[70:71], v[50:51] op_sel_hi:[0,1,1]
	v_pk_fma_f32 v[44:45], v[42:43], s[72:73], v[44:45] op_sel:[1,0,0]
	v_pk_fma_f32 v[46:47], v[42:43], s[74:75], v[46:47] op_sel:[1,0,0]
	v_pk_fma_f32 v[48:49], v[42:43], s[76:77], v[48:49] op_sel:[1,0,0]
	v_pk_fma_f32 v[50:51], v[42:43], s[78:79], v[50:51] op_sel:[1,0,0]
	global_store_dwordx4 v60, v[52:55], s[36:37] offset:16
	ds_write_b128 v61, v[44:47]
	ds_write_b128 v61, v[48:51] offset:16
	s_or_b64 exec, exec, s[38:39]
	s_waitcnt lgkmcnt(0)
	s_waitcnt vmcnt(2)
	s_branch .Lc7_cnt
.Ln0b_skip:
	s_or_b64 exec, exec, s[38:39]
	s_waitcnt vmcnt(0)
.Lc7_cnt:
	v_cmp_lt_i32_e64 s[10:11], -1, v9
	s_and_saveexec_b64 s[4:5], s[10:11]
	s_cbranch_execnz .LBB2_49

.LBB2_13:
	s_or_b64 exec, exec, s[4:5]
	v_cmp_lt_i32_e64 s[4:5], -1, v1
	s_and_saveexec_b64 s[12:13], s[4:5]

.LBB2_47:
	s_or_b64 exec, exec, s[6:7]
	s_and_saveexec_b64 s[42:43], s[40:41]
	v_mov_b32_e32 v28, 2
	v_lshlrev_b32_sdwa v28, v28, v27 dst_sel:DWORD dst_unused:UNUSED_PAD src0_sel:DWORD src1_sel:BYTE_0
	v_mov_b32_e32 v29, 1
	ds_add_rtn_u32 v28, v28, v29 offset:4864
	v_lshrrev_b32_e32 v30, 8, v27
	s_waitcnt lgkmcnt(0)
	v_ashrrev_i32_e32 v29, 31, v28
	v_lshl_add_u64 v[28:29], v[28:29], 2, s[20:21]
	global_store_dword v[28:29], v30, off
	s_or_b64 exec, exec, s[42:43]
	s_andn2_b64 vcc, exec, s[18:19]
	s_cbranch_vccz .LBB2_56
	s_branch .LBB2_74
.LBB2_49:
	v_mov_b32_e32 v4, 2
	v_lshlrev_b32_sdwa v4, v4, v9 dst_sel:DWORD dst_unused:UNUSED_PAD src0_sel:DWORD src1_sel:BYTE_0
	v_mov_b32_e32 v5, 1
	ds_add_u32 v4, v5 offset:4864
	s_or_b64 exec, exec, s[4:5]
	v_cmp_lt_i32_e64 s[8:9], -1, v8
	s_and_saveexec_b64 s[4:5], s[8:9]
	s_cbranch_execz .LBB2_12

.LBB2_51:
	v_mov_b32_e32 v4, 2
	v_lshlrev_b32_sdwa v4, v4, v3 dst_sel:DWORD dst_unused:UNUSED_PAD src0_sel:DWORD src1_sel:BYTE_0
	v_mov_b32_e32 v5, 1
	ds_add_u32 v4, v5 offset:4864
	s_or_b64 exec, exec, s[4:5]
	v_cmp_lt_i32_e64 s[4:5], -1, v1
	s_and_saveexec_b64 s[12:13], s[4:5]
	s_cbranch_execnz .LBB2_14
	s_branch .LBB2_15
